# v21: v19 + final combine/rmsnorm row loop rewritten by hand: 8 consecutive columns per lane (30 memory instr per row instead of 51) and next row's indices/x2 prefetched
# baseline (speedup 1.0000x reference)
; #define LAS __attribute__((address_space(3)))
; __device__ __forceinline__ void p12_final(const Frame& F, const KArgs& a) {
;     unsigned char* ws = F.ws; const int lane = F.lane; const LAS int* tab = (const LAS int*)(F.lds + LDS_TAB);
;     const unsigned short* X2 = (const unsigned short*)(ws + WS_X2B); const unsigned char* YB = ws + WS_YB; const int* TOPE = (const int*)(ws + WS_TOPE); const int* TOPR = (const int*)(ws + WS_TOPR);
;     for (int row = F.gw; row < NTOK; row += F.NGW) {
;         size_t so[4];
; #pragma unroll
;         for (int k = 0; k < 4; ++k) { const int e = TOPE[row * 4 + k], r = TOPR[row * 4 + k]; so[k] = (size_t)(tab[e] * 256 + r) * DM; }
;         f32x4 v[8]; float q = 0.f;
; #pragma unroll
;         for (int j = 0; j < 8; ++j) { const int c = 4 * (lane + 64 * j); { const u32x2 xr = *(const u32x2*)(X2 + (size_t)row * DM + c); v[j] = (f32x4){__builtin_bit_cast(float, xr.x << 16), __builtin_bit_cast(float, xr.x & 0xffff0000u), __builtin_bit_cast(float, xr.y << 16), __builtin_bit_cast(float, xr.y & 0xffff0000u)}; }
; #pragma unroll
;             for (int k = 0; k < 4; ++k) { const int y = *(const int*)(YB + so[k] + c);
.LBB0_2097:
	s_or_b64 exec, exec, s[0:1]
	v_readlane_b32 s0, v251, 1
	s_cmpk_gt_i32 s0, 0x3fff
	s_waitcnt lgkmcnt(0)
	s_barrier
	v_readlane_b32 s1, v251, 2
	s_cbranch_scc1 .LBB0_2100
	v_lshlrev_b32_e32 v2, 3, v198
	v_lshlrev_b32_e32 v3, 4, v198
	v_lshlrev_b32_e32 v4, 5, v198
	v_mov_b32_e32 v5, 0
	v_mov_b32_e32 v104, 0x358637bd
	s_add_u32 s8, s72, 0x39e00000
	s_addc_u32 s9, s73, 0
	s_add_u32 s10, s72, 0x39f00000
	s_addc_u32 s11, s73, 0
	s_add_u32 s0, s72, 0x4c500000
	s_addc_u32 s1, s73, 0
	s_add_u32 s2, s72, 0x35c00000
	s_addc_u32 s3, s73, 0
	v_readlane_b32 s4, v252, 2
	v_readlane_b32 s5, v252, 3
	v_readlane_b32 s6, v252, 4
	v_readlane_b32 s7, v252, 5
	v_readlane_b32 s20, v251, 1
	s_lshl_b32 s12, s20, 4
	s_add_u32 s14, s8, s12
	s_addc_u32 s15, s9, 0
	s_add_u32 s16, s10, s12
	s_addc_u32 s17, s11, 0
	global_load_dwordx4 v[8:11], v5, s[14:15]
	global_load_dwordx4 v[12:15], v5, s[16:17]
	s_lshl_b32 s12, s20, 12
	s_add_u32 s14, s2, s12
	s_addc_u32 s15, s3, 0
	global_load_dwordx4 v[16:19], v3, s[14:15]
	global_load_dwordx4 v[20:23], v3, s[14:15] offset:1024
	global_load_dwordx4 v[24:27], v3, s[14:15] offset:2048
	global_load_dwordx4 v[28:31], v3, s[14:15] offset:3072
	s_add_u32 s22, s4, 0x1000
	s_addc_u32 s23, s5, 0
	global_load_dwordx4 v[200:203], v4, s[4:5]
	global_load_dwordx4 v[204:207], v4, s[4:5] offset:16
	global_load_dwordx4 v[208:211], v4, s[4:5] offset:2048
	global_load_dwordx4 v[212:215], v4, s[4:5] offset:2064
	global_load_dwordx4 v[216:219], v4, s[22:23]
	global_load_dwordx4 v[220:223], v4, s[22:23] offset:16
	global_load_dwordx4 v[224:227], v4, s[22:23] offset:2048
	global_load_dwordx4 v[228:231], v4, s[22:23] offset:2064
	s_waitcnt vmcnt(0)
.Lp12_row:
	s_lshl_b32 s12, s20, 13
	s_add_u32 s18, s6, s12
	s_addc_u32 s19, s7, 0
	s_add_u32 s24, s18, 0x1000
	s_addc_u32 s25, s19, 0
	s_add_i32 s21, s20, s94
	s_waitcnt vmcnt(13)
	v_lshlrev_b32_e32 v8, 2, v8
	v_lshlrev_b32_e32 v9, 2, v9
	v_lshlrev_b32_e32 v10, 2, v10
	v_lshlrev_b32_e32 v11, 2, v11
	v_add_u32_e32 v8, 0x20100, v8
	v_add_u32_e32 v9, 0x20100, v9
	v_add_u32_e32 v10, 0x20100, v10
	v_add_u32_e32 v11, 0x20100, v11
	ds_read_b32 v8, v8
	ds_read_b32 v9, v9
	ds_read_b32 v10, v10
	ds_read_b32 v11, v11
	s_waitcnt vmcnt(12) lgkmcnt(0)
	v_lshl_add_u32 v8, v8, 8, v12
	v_lshl_add_u32 v9, v9, 8, v13
	v_lshl_add_u32 v10, v10, 8, v14
	v_lshl_add_u32 v11, v11, 8, v15
	v_lshl_add_u32 v8, v8, 11, v2
	v_lshl_add_u32 v9, v9, 11, v2
	v_lshl_add_u32 v10, v10, 11, v2
	v_lshl_add_u32 v11, v11, 11, v2
	global_load_dwordx2 v[32:33], v8, s[0:1]
	global_load_dwordx2 v[40:41], v9, s[0:1]
	global_load_dwordx2 v[48:49], v10, s[0:1]
	global_load_dwordx2 v[56:57], v11, s[0:1]
	global_load_dwordx2 v[34:35], v8, s[0:1] offset:512
	global_load_dwordx2 v[42:43], v9, s[0:1] offset:512
	global_load_dwordx2 v[50:51], v10, s[0:1] offset:512
	global_load_dwordx2 v[58:59], v11, s[0:1] offset:512
	global_load_dwordx2 v[36:37], v8, s[0:1] offset:1024
	global_load_dwordx2 v[44:45], v9, s[0:1] offset:1024
	global_load_dwordx2 v[52:53], v10, s[0:1] offset:1024
	global_load_dwordx2 v[60:61], v11, s[0:1] offset:1024
	global_load_dwordx2 v[38:39], v8, s[0:1] offset:1536
	global_load_dwordx2 v[46:47], v9, s[0:1] offset:1536
	global_load_dwordx2 v[54:55], v10, s[0:1] offset:1536
	global_load_dwordx2 v[62:63], v11, s[0:1] offset:1536
	s_lshl_b32 s12, s21, 4
	s_add_u32 s14, s8, s12
	s_addc_u32 s15, s9, 0
	s_add_u32 s16, s10, s12
	s_addc_u32 s17, s11, 0
	global_load_dwordx4 v[110:113], v5, s[14:15]
	global_load_dwordx4 v[114:117], v5, s[16:17]
	s_lshl_b32 s12, s21, 12
	s_add_u32 s14, s2, s12
	s_addc_u32 s15, s3, 0
	global_load_dwordx4 v[118:121], v3, s[14:15]
	global_load_dwordx4 v[122:125], v3, s[14:15] offset:1024
	global_load_dwordx4 v[126:129], v3, s[14:15] offset:2048
	global_load_dwordx4 v[130:133], v3, s[14:15] offset:3072
	s_waitcnt vmcnt(30)
	v_lshlrev_b32_e32 v64, 16, v16
	v_and_b32_e32 v65, 0xffff0000, v16
	v_lshlrev_b32_e32 v66, 16, v17
	v_and_b32_e32 v67, 0xffff0000, v17
	v_lshlrev_b32_e32 v68, 16, v18
	v_and_b32_e32 v69, 0xffff0000, v18
	v_lshlrev_b32_e32 v70, 16, v19
	v_and_b32_e32 v71, 0xffff0000, v19
	v_lshlrev_b32_e32 v72, 16, v20
	v_and_b32_e32 v73, 0xffff0000, v20
	v_lshlrev_b32_e32 v74, 16, v21
	v_and_b32_e32 v75, 0xffff0000, v21
	v_lshlrev_b32_e32 v76, 16, v22
	v_and_b32_e32 v77, 0xffff0000, v22
	v_lshlrev_b32_e32 v78, 16, v23
	v_and_b32_e32 v79, 0xffff0000, v23
	v_lshlrev_b32_e32 v80, 16, v24
	v_and_b32_e32 v81, 0xffff0000, v24
	v_lshlrev_b32_e32 v82, 16, v25
	v_and_b32_e32 v83, 0xffff0000, v25
	v_lshlrev_b32_e32 v84, 16, v26
	v_and_b32_e32 v85, 0xffff0000, v26
	v_lshlrev_b32_e32 v86, 16, v27
	v_and_b32_e32 v87, 0xffff0000, v27
	v_lshlrev_b32_e32 v88, 16, v28
	v_and_b32_e32 v89, 0xffff0000, v28
	v_lshlrev_b32_e32 v90, 16, v29
	v_and_b32_e32 v91, 0xffff0000, v29
	v_lshlrev_b32_e32 v92, 16, v30
	v_and_b32_e32 v93, 0xffff0000, v30
	v_lshlrev_b32_e32 v94, 16, v31
	v_and_b32_e32 v95, 0xffff0000, v31
	s_waitcnt vmcnt(18)
; __device__ __forceinline__ void p12_final(const Frame& F, const KArgs& a) {
;     ...
;         for (int j = 0; j < 8; ++j) { const int c = 4 * (lane + 64 * j); { const u32x2 xr = *(const u32x2*)(X2 + (size_t)row * DM + c); v[j] = (f32x4){__builtin_bit_cast(float, xr.x << 16), __builtin_bit_cast(float, xr.x & 0xffff0000u), __builtin_bit_cast(float, xr.y << 16), __builtin_bit_cast(float, xr.y & 0xffff0000u)}; }
; #pragma unroll
;             for (int k = 0; k < 4; ++k) { const int y = *(const int*)(YB + so[k] + c);
;                 v[j][0] += __builtin_amdgcn_cvt_f32_fp8(y, 0); v[j][1] += __builtin_amdgcn_cvt_f32_fp8(y, 1); v[j][2] += __builtin_amdgcn_cvt_f32_fp8(y, 2); v[j][3] += __builtin_amdgcn_cvt_f32_fp8(y, 3); }
;             q += (v[j][0] * v[j][0] + v[j][1] * v[j][1]) + (v[j][2] * v[j][2] + v[j][3] * v[j][3]); }
	v_cvt_f32_fp8_e32 v96, v32
	v_cvt_f32_fp8_sdwa v97, v32 src0_sel:BYTE_1
	v_cvt_f32_fp8_sdwa v98, v32 src0_sel:BYTE_2
	v_cvt_f32_fp8_sdwa v99, v32 src0_sel:BYTE_3
	v_cvt_f32_fp8_e32 v100, v33
	v_cvt_f32_fp8_sdwa v101, v33 src0_sel:BYTE_1
	v_cvt_f32_fp8_sdwa v102, v33 src0_sel:BYTE_2
	v_cvt_f32_fp8_sdwa v103, v33 src0_sel:BYTE_3
	v_pk_add_f32 v[64:65], v[64:65], v[96:97]
	v_pk_add_f32 v[66:67], v[66:67], v[98:99]
	v_pk_add_f32 v[68:69], v[68:69], v[100:101]
	v_pk_add_f32 v[70:71], v[70:71], v[102:103]
	v_cvt_f32_fp8_e32 v96, v40
	v_cvt_f32_fp8_sdwa v97, v40 src0_sel:BYTE_1
	v_cvt_f32_fp8_sdwa v98, v40 src0_sel:BYTE_2
	v_cvt_f32_fp8_sdwa v99, v40 src0_sel:BYTE_3
	v_cvt_f32_fp8_e32 v100, v41
	v_cvt_f32_fp8_sdwa v101, v41 src0_sel:BYTE_1
	v_cvt_f32_fp8_sdwa v102, v41 src0_sel:BYTE_2
	v_cvt_f32_fp8_sdwa v103, v41 src0_sel:BYTE_3
	v_pk_add_f32 v[64:65], v[64:65], v[96:97]
	v_pk_add_f32 v[66:67], v[66:67], v[98:99]
	v_pk_add_f32 v[68:69], v[68:69], v[100:101]
	v_pk_add_f32 v[70:71], v[70:71], v[102:103]
	v_cvt_f32_fp8_e32 v96, v48
	v_cvt_f32_fp8_sdwa v97, v48 src0_sel:BYTE_1
	v_cvt_f32_fp8_sdwa v98, v48 src0_sel:BYTE_2
	v_cvt_f32_fp8_sdwa v99, v48 src0_sel:BYTE_3
	v_cvt_f32_fp8_e32 v100, v49
	v_cvt_f32_fp8_sdwa v101, v49 src0_sel:BYTE_1
	v_cvt_f32_fp8_sdwa v102, v49 src0_sel:BYTE_2
	v_cvt_f32_fp8_sdwa v103, v49 src0_sel:BYTE_3
	v_pk_add_f32 v[64:65], v[64:65], v[96:97]
	v_pk_add_f32 v[66:67], v[66:67], v[98:99]
	v_pk_add_f32 v[68:69], v[68:69], v[100:101]
	v_pk_add_f32 v[70:71], v[70:71], v[102:103]
	v_cvt_f32_fp8_e32 v96, v56
	v_cvt_f32_fp8_sdwa v97, v56 src0_sel:BYTE_1
	v_cvt_f32_fp8_sdwa v98, v56 src0_sel:BYTE_2
	v_cvt_f32_fp8_sdwa v99, v56 src0_sel:BYTE_3
	v_cvt_f32_fp8_e32 v100, v57
	v_cvt_f32_fp8_sdwa v101, v57 src0_sel:BYTE_1
	v_cvt_f32_fp8_sdwa v102, v57 src0_sel:BYTE_2
	v_cvt_f32_fp8_sdwa v103, v57 src0_sel:BYTE_3
	v_pk_add_f32 v[64:65], v[64:65], v[96:97]
	v_pk_add_f32 v[66:67], v[66:67], v[98:99]
	v_pk_add_f32 v[68:69], v[68:69], v[100:101]
	v_pk_add_f32 v[70:71], v[70:71], v[102:103]
	s_waitcnt vmcnt(14)
	v_cvt_f32_fp8_e32 v96, v34
	v_cvt_f32_fp8_sdwa v97, v34 src0_sel:BYTE_1
	v_cvt_f32_fp8_sdwa v98, v34 src0_sel:BYTE_2
	v_cvt_f32_fp8_sdwa v99, v34 src0_sel:BYTE_3
	v_cvt_f32_fp8_e32 v100, v35
	v_cvt_f32_fp8_sdwa v101, v35 src0_sel:BYTE_1
	v_cvt_f32_fp8_sdwa v102, v35 src0_sel:BYTE_2
	v_cvt_f32_fp8_sdwa v103, v35 src0_sel:BYTE_3
	v_pk_add_f32 v[72:73], v[72:73], v[96:97]
	v_pk_add_f32 v[74:75], v[74:75], v[98:99]
	v_pk_add_f32 v[76:77], v[76:77], v[100:101]
	v_pk_add_f32 v[78:79], v[78:79], v[102:103]
	v_cvt_f32_fp8_e32 v96, v42
	v_cvt_f32_fp8_sdwa v97, v42 src0_sel:BYTE_1
	v_cvt_f32_fp8_sdwa v98, v42 src0_sel:BYTE_2
	v_cvt_f32_fp8_sdwa v99, v42 src0_sel:BYTE_3
	v_cvt_f32_fp8_e32 v100, v43
	v_cvt_f32_fp8_sdwa v101, v43 src0_sel:BYTE_1
	v_cvt_f32_fp8_sdwa v102, v43 src0_sel:BYTE_2
	v_cvt_f32_fp8_sdwa v103, v43 src0_sel:BYTE_3
	v_pk_add_f32 v[72:73], v[72:73], v[96:97]
	v_pk_add_f32 v[74:75], v[74:75], v[98:99]
	v_pk_add_f32 v[76:77], v[76:77], v[100:101]
	v_pk_add_f32 v[78:79], v[78:79], v[102:103]
	v_cvt_f32_fp8_e32 v96, v50
	v_cvt_f32_fp8_sdwa v97, v50 src0_sel:BYTE_1
	v_cvt_f32_fp8_sdwa v98, v50 src0_sel:BYTE_2
	v_cvt_f32_fp8_sdwa v99, v50 src0_sel:BYTE_3
	v_cvt_f32_fp8_e32 v100, v51
	v_cvt_f32_fp8_sdwa v101, v51 src0_sel:BYTE_1
	v_cvt_f32_fp8_sdwa v102, v51 src0_sel:BYTE_2
	v_cvt_f32_fp8_sdwa v103, v51 src0_sel:BYTE_3
	v_pk_add_f32 v[72:73], v[72:73], v[96:97]
	v_pk_add_f32 v[74:75], v[74:75], v[98:99]
	v_pk_add_f32 v[76:77], v[76:77], v[100:101]
	v_pk_add_f32 v[78:79], v[78:79], v[102:103]
	v_cvt_f32_fp8_e32 v96, v58
	v_cvt_f32_fp8_sdwa v97, v58 src0_sel:BYTE_1
	v_cvt_f32_fp8_sdwa v98, v58 src0_sel:BYTE_2
	v_cvt_f32_fp8_sdwa v99, v58 src0_sel:BYTE_3
	v_cvt_f32_fp8_e32 v100, v59
	v_cvt_f32_fp8_sdwa v101, v59 src0_sel:BYTE_1
	v_cvt_f32_fp8_sdwa v102, v59 src0_sel:BYTE_2
	v_cvt_f32_fp8_sdwa v103, v59 src0_sel:BYTE_3
	v_pk_add_f32 v[72:73], v[72:73], v[96:97]
	v_pk_add_f32 v[74:75], v[74:75], v[98:99]
	v_pk_add_f32 v[76:77], v[76:77], v[100:101]
	v_pk_add_f32 v[78:79], v[78:79], v[102:103]
	s_waitcnt vmcnt(10)
	v_cvt_f32_fp8_e32 v96, v36
	v_cvt_f32_fp8_sdwa v97, v36 src0_sel:BYTE_1
	v_cvt_f32_fp8_sdwa v98, v36 src0_sel:BYTE_2
	v_cvt_f32_fp8_sdwa v99, v36 src0_sel:BYTE_3
	v_cvt_f32_fp8_e32 v100, v37
	v_cvt_f32_fp8_sdwa v101, v37 src0_sel:BYTE_1
	v_cvt_f32_fp8_sdwa v102, v37 src0_sel:BYTE_2
	v_cvt_f32_fp8_sdwa v103, v37 src0_sel:BYTE_3
	v_pk_add_f32 v[80:81], v[80:81], v[96:97]
	v_pk_add_f32 v[82:83], v[82:83], v[98:99]
	v_pk_add_f32 v[84:85], v[84:85], v[100:101]
	v_pk_add_f32 v[86:87], v[86:87], v[102:103]
	v_cvt_f32_fp8_e32 v96, v44
	v_cvt_f32_fp8_sdwa v97, v44 src0_sel:BYTE_1
	v_cvt_f32_fp8_sdwa v98, v44 src0_sel:BYTE_2
	v_cvt_f32_fp8_sdwa v99, v44 src0_sel:BYTE_3
	v_cvt_f32_fp8_e32 v100, v45
	v_cvt_f32_fp8_sdwa v101, v45 src0_sel:BYTE_1
	v_cvt_f32_fp8_sdwa v102, v45 src0_sel:BYTE_2
	v_cvt_f32_fp8_sdwa v103, v45 src0_sel:BYTE_3
	v_pk_add_f32 v[80:81], v[80:81], v[96:97]
	v_pk_add_f32 v[82:83], v[82:83], v[98:99]
	v_pk_add_f32 v[84:85], v[84:85], v[100:101]
	v_pk_add_f32 v[86:87], v[86:87], v[102:103]
	v_cvt_f32_fp8_e32 v96, v52
	v_cvt_f32_fp8_sdwa v97, v52 src0_sel:BYTE_1
	v_cvt_f32_fp8_sdwa v98, v52 src0_sel:BYTE_2
	v_cvt_f32_fp8_sdwa v99, v52 src0_sel:BYTE_3
	v_cvt_f32_fp8_e32 v100, v53
	v_cvt_f32_fp8_sdwa v101, v53 src0_sel:BYTE_1
	v_cvt_f32_fp8_sdwa v102, v53 src0_sel:BYTE_2
	v_cvt_f32_fp8_sdwa v103, v53 src0_sel:BYTE_3
	v_pk_add_f32 v[80:81], v[80:81], v[96:97]
	v_pk_add_f32 v[82:83], v[82:83], v[98:99]
	v_pk_add_f32 v[84:85], v[84:85], v[100:101]
	v_pk_add_f32 v[86:87], v[86:87], v[102:103]
	v_cvt_f32_fp8_e32 v96, v60
	v_cvt_f32_fp8_sdwa v97, v60 src0_sel:BYTE_1
	v_cvt_f32_fp8_sdwa v98, v60 src0_sel:BYTE_2
	v_cvt_f32_fp8_sdwa v99, v60 src0_sel:BYTE_3
	v_cvt_f32_fp8_e32 v100, v61
	v_cvt_f32_fp8_sdwa v101, v61 src0_sel:BYTE_1
	v_cvt_f32_fp8_sdwa v102, v61 src0_sel:BYTE_2
	v_cvt_f32_fp8_sdwa v103, v61 src0_sel:BYTE_3
	v_pk_add_f32 v[80:81], v[80:81], v[96:97]
	v_pk_add_f32 v[82:83], v[82:83], v[98:99]
	v_pk_add_f32 v[84:85], v[84:85], v[100:101]
	v_pk_add_f32 v[86:87], v[86:87], v[102:103]
	s_waitcnt vmcnt(6)
; __device__ __forceinline__ void p12_final(const Frame& F, const KArgs& a) {
;     ...
;             q += (v[j][0] * v[j][0] + v[j][1] * v[j][1]) + (v[j][2] * v[j][2] + v[j][3] * v[j][3]); }
;         const float rs = rsqrtf(wave_sum(q) * (1.f / DM) + RMS_EPS);
; #pragma unroll
;         for (int j = 0; j < 8; ++j) { const int c = 4 * (lane + 64 * j); const f32x4 g = *(const f32x4*)(a.in[24] + c); *(f32x4*)(a.out + (size_t)row * DM + c) = v[j] * rs * g; }
	v_cvt_f32_fp8_e32 v96, v38
	v_cvt_f32_fp8_sdwa v97, v38 src0_sel:BYTE_1
	v_cvt_f32_fp8_sdwa v98, v38 src0_sel:BYTE_2
	v_cvt_f32_fp8_sdwa v99, v38 src0_sel:BYTE_3
	v_cvt_f32_fp8_e32 v100, v39
	v_cvt_f32_fp8_sdwa v101, v39 src0_sel:BYTE_1
	v_cvt_f32_fp8_sdwa v102, v39 src0_sel:BYTE_2
	v_cvt_f32_fp8_sdwa v103, v39 src0_sel:BYTE_3
	v_pk_add_f32 v[88:89], v[88:89], v[96:97]
	v_pk_add_f32 v[90:91], v[90:91], v[98:99]
	v_pk_add_f32 v[92:93], v[92:93], v[100:101]
	v_pk_add_f32 v[94:95], v[94:95], v[102:103]
	v_cvt_f32_fp8_e32 v96, v46
	v_cvt_f32_fp8_sdwa v97, v46 src0_sel:BYTE_1
	v_cvt_f32_fp8_sdwa v98, v46 src0_sel:BYTE_2
	v_cvt_f32_fp8_sdwa v99, v46 src0_sel:BYTE_3
	v_cvt_f32_fp8_e32 v100, v47
	v_cvt_f32_fp8_sdwa v101, v47 src0_sel:BYTE_1
	v_cvt_f32_fp8_sdwa v102, v47 src0_sel:BYTE_2
	v_cvt_f32_fp8_sdwa v103, v47 src0_sel:BYTE_3
	v_pk_add_f32 v[88:89], v[88:89], v[96:97]
	v_pk_add_f32 v[90:91], v[90:91], v[98:99]
	v_pk_add_f32 v[92:93], v[92:93], v[100:101]
	v_pk_add_f32 v[94:95], v[94:95], v[102:103]
	v_cvt_f32_fp8_e32 v96, v54
	v_cvt_f32_fp8_sdwa v97, v54 src0_sel:BYTE_1
	v_cvt_f32_fp8_sdwa v98, v54 src0_sel:BYTE_2
	v_cvt_f32_fp8_sdwa v99, v54 src0_sel:BYTE_3
	v_cvt_f32_fp8_e32 v100, v55
	v_cvt_f32_fp8_sdwa v101, v55 src0_sel:BYTE_1
	v_cvt_f32_fp8_sdwa v102, v55 src0_sel:BYTE_2
	v_cvt_f32_fp8_sdwa v103, v55 src0_sel:BYTE_3
	v_pk_add_f32 v[88:89], v[88:89], v[96:97]
	v_pk_add_f32 v[90:91], v[90:91], v[98:99]
	v_pk_add_f32 v[92:93], v[92:93], v[100:101]
	v_pk_add_f32 v[94:95], v[94:95], v[102:103]
	v_cvt_f32_fp8_e32 v96, v62
	v_cvt_f32_fp8_sdwa v97, v62 src0_sel:BYTE_1
	v_cvt_f32_fp8_sdwa v98, v62 src0_sel:BYTE_2
	v_cvt_f32_fp8_sdwa v99, v62 src0_sel:BYTE_3
	v_cvt_f32_fp8_e32 v100, v63
	v_cvt_f32_fp8_sdwa v101, v63 src0_sel:BYTE_1
	v_cvt_f32_fp8_sdwa v102, v63 src0_sel:BYTE_2
	v_cvt_f32_fp8_sdwa v103, v63 src0_sel:BYTE_3
	v_pk_add_f32 v[88:89], v[88:89], v[96:97]
	v_pk_add_f32 v[90:91], v[90:91], v[98:99]
	v_pk_add_f32 v[92:93], v[92:93], v[100:101]
	v_pk_add_f32 v[94:95], v[94:95], v[102:103]
	v_pk_mul_f32 v[106:107], v[64:65], v[64:65]
	v_pk_fma_f32 v[106:107], v[66:67], v[66:67], v[106:107]
	v_pk_fma_f32 v[106:107], v[68:69], v[68:69], v[106:107]
	v_pk_fma_f32 v[106:107], v[70:71], v[70:71], v[106:107]
	v_pk_fma_f32 v[106:107], v[72:73], v[72:73], v[106:107]
	v_pk_fma_f32 v[106:107], v[74:75], v[74:75], v[106:107]
	v_pk_fma_f32 v[106:107], v[76:77], v[76:77], v[106:107]
	v_pk_fma_f32 v[106:107], v[78:79], v[78:79], v[106:107]
	v_pk_fma_f32 v[106:107], v[80:81], v[80:81], v[106:107]
	v_pk_fma_f32 v[106:107], v[82:83], v[82:83], v[106:107]
	v_pk_fma_f32 v[106:107], v[84:85], v[84:85], v[106:107]
	v_pk_fma_f32 v[106:107], v[86:87], v[86:87], v[106:107]
	v_pk_fma_f32 v[106:107], v[88:89], v[88:89], v[106:107]
	v_pk_fma_f32 v[106:107], v[90:91], v[90:91], v[106:107]
	v_pk_fma_f32 v[106:107], v[92:93], v[92:93], v[106:107]
	v_pk_fma_f32 v[106:107], v[94:95], v[94:95], v[106:107]
	s_nop 0
	v_add_f32_e32 v105, v106, v107
	s_nop 1
	v_add_f32_dpp v105, v105, v105 quad_perm:[1,0,3,2] row_mask:0xf bank_mask:0xf
	s_nop 1
	v_add_f32_dpp v105, v105, v105 quad_perm:[2,3,0,1] row_mask:0xf bank_mask:0xf
	s_nop 1
	v_add_f32_dpp v105, v105, v105 row_half_mirror row_mask:0xf bank_mask:0xf
	s_nop 1
	v_add_f32_dpp v105, v105, v105 row_mirror row_mask:0xf bank_mask:0xf
	s_nop 1
	v_readlane_b32 s12, v105, 0
	v_readlane_b32 s14, v105, 16
	v_readlane_b32 s15, v105, 32
	v_readlane_b32 s16, v105, 48
	s_nop 1
	v_mov_b32_e32 v105, s12
	v_add_f32_e32 v105, s14, v105
	v_add_f32_e32 v105, s15, v105
	v_add_f32_e32 v105, s16, v105
	v_fmamk_f32 v105, v105, 0x3a000000, v104
	v_rsq_f32_e32 v108, v105
	s_nop 0
	v_pk_mul_f32 v[64:65], v[64:65], v[108:109] op_sel_hi:[1,0]
	v_pk_mul_f32 v[66:67], v[66:67], v[108:109] op_sel_hi:[1,0]
	v_pk_mul_f32 v[68:69], v[68:69], v[108:109] op_sel_hi:[1,0]
	v_pk_mul_f32 v[70:71], v[70:71], v[108:109] op_sel_hi:[1,0]
	v_pk_mul_f32 v[64:65], v[64:65], v[200:201]
	v_pk_mul_f32 v[66:67], v[66:67], v[202:203]
	v_pk_mul_f32 v[68:69], v[68:69], v[204:205]
	v_pk_mul_f32 v[70:71], v[70:71], v[206:207]
	global_store_dwordx4 v4, v[64:67], s[18:19]
	global_store_dwordx4 v4, v[68:71], s[18:19] offset:16
	v_pk_mul_f32 v[72:73], v[72:73], v[108:109] op_sel_hi:[1,0]
	v_pk_mul_f32 v[74:75], v[74:75], v[108:109] op_sel_hi:[1,0]
	v_pk_mul_f32 v[76:77], v[76:77], v[108:109] op_sel_hi:[1,0]
	v_pk_mul_f32 v[78:79], v[78:79], v[108:109] op_sel_hi:[1,0]
	v_pk_mul_f32 v[72:73], v[72:73], v[208:209]
	v_pk_mul_f32 v[74:75], v[74:75], v[210:211]
	v_pk_mul_f32 v[76:77], v[76:77], v[212:213]
	v_pk_mul_f32 v[78:79], v[78:79], v[214:215]
	global_store_dwordx4 v4, v[72:75], s[18:19] offset:2048
	global_store_dwordx4 v4, v[76:79], s[18:19] offset:2064
	v_pk_mul_f32 v[80:81], v[80:81], v[108:109] op_sel_hi:[1,0]
	v_pk_mul_f32 v[82:83], v[82:83], v[108:109] op_sel_hi:[1,0]
	v_pk_mul_f32 v[84:85], v[84:85], v[108:109] op_sel_hi:[1,0]
	v_pk_mul_f32 v[86:87], v[86:87], v[108:109] op_sel_hi:[1,0]
	v_pk_mul_f32 v[80:81], v[80:81], v[216:217]
	v_pk_mul_f32 v[82:83], v[82:83], v[218:219]
	v_pk_mul_f32 v[84:85], v[84:85], v[220:221]
	v_pk_mul_f32 v[86:87], v[86:87], v[222:223]
	global_store_dwordx4 v4, v[80:83], s[24:25]
	global_store_dwordx4 v4, v[84:87], s[24:25] offset:16
	v_pk_mul_f32 v[88:89], v[88:89], v[108:109] op_sel_hi:[1,0]
	v_pk_mul_f32 v[90:91], v[90:91], v[108:109] op_sel_hi:[1,0]
	v_pk_mul_f32 v[92:93], v[92:93], v[108:109] op_sel_hi:[1,0]
	v_pk_mul_f32 v[94:95], v[94:95], v[108:109] op_sel_hi:[1,0]
	v_pk_mul_f32 v[88:89], v[88:89], v[224:225]
	v_pk_mul_f32 v[90:91], v[90:91], v[226:227]
	v_pk_mul_f32 v[92:93], v[92:93], v[228:229]
	v_pk_mul_f32 v[94:95], v[94:95], v[230:231]
	global_store_dwordx4 v4, v[88:91], s[24:25] offset:2048
	global_store_dwordx4 v4, v[92:95], s[24:25] offset:2064
	s_mov_b32 s20, s21
	s_lshl_b32 s12, s20, 13
	s_add_u32 s18, s6, s12
	s_addc_u32 s19, s7, 0
	s_add_u32 s24, s18, 0x1000
	s_addc_u32 s25, s19, 0
	s_add_i32 s21, s20, s94
	s_waitcnt vmcnt(13)
; __device__ __forceinline__ void p12_final(const Frame& F, const KArgs& a) {
;     ...
;     for (int row = F.gw; row < NTOK; row += F.NGW) {
;         size_t so[4];
; #pragma unroll
;         for (int k = 0; k < 4; ++k) { const int e = TOPE[row * 4 + k], r = TOPR[row * 4 + k]; so[k] = (size_t)(tab[e] * 256 + r) * DM; }
;         f32x4 v[8]; float q = 0.f;
; #pragma unroll
;         for (int j = 0; j < 8; ++j) { const int c = 4 * (lane + 64 * j); { const u32x2 xr = *(const u32x2*)(X2 + (size_t)row * DM + c); v[j] = (f32x4){__builtin_bit_cast(float, xr.x << 16), __builtin_bit_cast(float, xr.x & 0xffff0000u), __builtin_bit_cast(float, xr.y << 16), __builtin_bit_cast(float, xr.y & 0xffff0000u)}; }
; #pragma unroll
;             for (int k = 0; k < 4; ++k) { const int y = *(const int*)(YB + so[k] + c);
;                 v[j][0] += __builtin_amdgcn_cvt_f32_fp8(y, 0); v[j][1] += __builtin_amdgcn_cvt_f32_fp8(y, 1); v[j][2] += __builtin_amdgcn_cvt_f32_fp8(y, 2); v[j][3] += __builtin_amdgcn_cvt_f32_fp8(y, 3); }
;             q += (v[j][0] * v[j][0] + v[j][1] * v[j][1]) + (v[j][2] * v[j][2] + v[j][3] * v[j][3]); }
	v_lshlrev_b32_e32 v110, 2, v110
	v_lshlrev_b32_e32 v111, 2, v111
	v_lshlrev_b32_e32 v112, 2, v112
	v_lshlrev_b32_e32 v113, 2, v113
	v_add_u32_e32 v110, 0x20100, v110
	v_add_u32_e32 v111, 0x20100, v111
	v_add_u32_e32 v112, 0x20100, v112
	v_add_u32_e32 v113, 0x20100, v113
	ds_read_b32 v110, v110
	ds_read_b32 v111, v111
	ds_read_b32 v112, v112
	ds_read_b32 v113, v113
	s_waitcnt vmcnt(12) lgkmcnt(0)
	v_lshl_add_u32 v110, v110, 8, v114
	v_lshl_add_u32 v111, v111, 8, v115
	v_lshl_add_u32 v112, v112, 8, v116
	v_lshl_add_u32 v113, v113, 8, v117
	v_lshl_add_u32 v110, v110, 11, v2
	v_lshl_add_u32 v111, v111, 11, v2
	v_lshl_add_u32 v112, v112, 11, v2
	v_lshl_add_u32 v113, v113, 11, v2
	global_load_dwordx2 v[32:33], v110, s[0:1]
	global_load_dwordx2 v[40:41], v111, s[0:1]
	global_load_dwordx2 v[48:49], v112, s[0:1]
	global_load_dwordx2 v[56:57], v113, s[0:1]
	global_load_dwordx2 v[34:35], v110, s[0:1] offset:512
	global_load_dwordx2 v[42:43], v111, s[0:1] offset:512
	global_load_dwordx2 v[50:51], v112, s[0:1] offset:512
	global_load_dwordx2 v[58:59], v113, s[0:1] offset:512
	global_load_dwordx2 v[36:37], v110, s[0:1] offset:1024
	global_load_dwordx2 v[44:45], v111, s[0:1] offset:1024
	global_load_dwordx2 v[52:53], v112, s[0:1] offset:1024
	global_load_dwordx2 v[60:61], v113, s[0:1] offset:1024
	global_load_dwordx2 v[38:39], v110, s[0:1] offset:1536
	global_load_dwordx2 v[46:47], v111, s[0:1] offset:1536
	global_load_dwordx2 v[54:55], v112, s[0:1] offset:1536
	global_load_dwordx2 v[62:63], v113, s[0:1] offset:1536
	s_lshl_b32 s12, s21, 4
	s_add_u32 s14, s8, s12
	s_addc_u32 s15, s9, 0
	s_add_u32 s16, s10, s12
	s_addc_u32 s17, s11, 0
	global_load_dwordx4 v[8:11], v5, s[14:15]
	global_load_dwordx4 v[12:15], v5, s[16:17]
	s_lshl_b32 s12, s21, 12
	s_add_u32 s14, s2, s12
	s_addc_u32 s15, s3, 0
	global_load_dwordx4 v[16:19], v3, s[14:15]
	global_load_dwordx4 v[20:23], v3, s[14:15] offset:1024
	global_load_dwordx4 v[24:27], v3, s[14:15] offset:2048
	global_load_dwordx4 v[28:31], v3, s[14:15] offset:3072
	s_waitcnt vmcnt(30)
	v_lshlrev_b32_e32 v64, 16, v118
	v_and_b32_e32 v65, 0xffff0000, v118
	v_lshlrev_b32_e32 v66, 16, v119
	v_and_b32_e32 v67, 0xffff0000, v119
	v_lshlrev_b32_e32 v68, 16, v120
	v_and_b32_e32 v69, 0xffff0000, v120
	v_lshlrev_b32_e32 v70, 16, v121
	v_and_b32_e32 v71, 0xffff0000, v121
	v_lshlrev_b32_e32 v72, 16, v122
	v_and_b32_e32 v73, 0xffff0000, v122
	v_lshlrev_b32_e32 v74, 16, v123
	v_and_b32_e32 v75, 0xffff0000, v123
	v_lshlrev_b32_e32 v76, 16, v124
	v_and_b32_e32 v77, 0xffff0000, v124
	v_lshlrev_b32_e32 v78, 16, v125
	v_and_b32_e32 v79, 0xffff0000, v125
	v_lshlrev_b32_e32 v80, 16, v126
	v_and_b32_e32 v81, 0xffff0000, v126
	v_lshlrev_b32_e32 v82, 16, v127
	v_and_b32_e32 v83, 0xffff0000, v127
	v_lshlrev_b32_e32 v84, 16, v128
	v_and_b32_e32 v85, 0xffff0000, v128
	v_lshlrev_b32_e32 v86, 16, v129
	v_and_b32_e32 v87, 0xffff0000, v129
	v_lshlrev_b32_e32 v88, 16, v130
	v_and_b32_e32 v89, 0xffff0000, v130
	v_lshlrev_b32_e32 v90, 16, v131
	v_and_b32_e32 v91, 0xffff0000, v131
	v_lshlrev_b32_e32 v92, 16, v132
	v_and_b32_e32 v93, 0xffff0000, v132
	v_lshlrev_b32_e32 v94, 16, v133
	v_and_b32_e32 v95, 0xffff0000, v133
	s_waitcnt vmcnt(18)
	v_cvt_f32_fp8_e32 v96, v32
	v_cvt_f32_fp8_sdwa v97, v32 src0_sel:BYTE_1
	v_cvt_f32_fp8_sdwa v98, v32 src0_sel:BYTE_2
	v_cvt_f32_fp8_sdwa v99, v32 src0_sel:BYTE_3
	v_cvt_f32_fp8_e32 v100, v33
	v_cvt_f32_fp8_sdwa v101, v33 src0_sel:BYTE_1
	v_cvt_f32_fp8_sdwa v102, v33 src0_sel:BYTE_2
	v_cvt_f32_fp8_sdwa v103, v33 src0_sel:BYTE_3
	v_pk_add_f32 v[64:65], v[64:65], v[96:97]
	v_pk_add_f32 v[66:67], v[66:67], v[98:99]
	v_pk_add_f32 v[68:69], v[68:69], v[100:101]
	v_pk_add_f32 v[70:71], v[70:71], v[102:103]
	v_cvt_f32_fp8_e32 v96, v40
	v_cvt_f32_fp8_sdwa v97, v40 src0_sel:BYTE_1
	v_cvt_f32_fp8_sdwa v98, v40 src0_sel:BYTE_2
	v_cvt_f32_fp8_sdwa v99, v40 src0_sel:BYTE_3
	v_cvt_f32_fp8_e32 v100, v41
	v_cvt_f32_fp8_sdwa v101, v41 src0_sel:BYTE_1
	v_cvt_f32_fp8_sdwa v102, v41 src0_sel:BYTE_2
	v_cvt_f32_fp8_sdwa v103, v41 src0_sel:BYTE_3
	v_pk_add_f32 v[64:65], v[64:65], v[96:97]
	v_pk_add_f32 v[66:67], v[66:67], v[98:99]
	v_pk_add_f32 v[68:69], v[68:69], v[100:101]
	v_pk_add_f32 v[70:71], v[70:71], v[102:103]
	v_cvt_f32_fp8_e32 v96, v48
	v_cvt_f32_fp8_sdwa v97, v48 src0_sel:BYTE_1
	v_cvt_f32_fp8_sdwa v98, v48 src0_sel:BYTE_2
	v_cvt_f32_fp8_sdwa v99, v48 src0_sel:BYTE_3
	v_cvt_f32_fp8_e32 v100, v49
	v_cvt_f32_fp8_sdwa v101, v49 src0_sel:BYTE_1
	v_cvt_f32_fp8_sdwa v102, v49 src0_sel:BYTE_2
	v_cvt_f32_fp8_sdwa v103, v49 src0_sel:BYTE_3
	v_pk_add_f32 v[64:65], v[64:65], v[96:97]
	v_pk_add_f32 v[66:67], v[66:67], v[98:99]
	v_pk_add_f32 v[68:69], v[68:69], v[100:101]
	v_pk_add_f32 v[70:71], v[70:71], v[102:103]
	v_cvt_f32_fp8_e32 v96, v56
	v_cvt_f32_fp8_sdwa v97, v56 src0_sel:BYTE_1
	v_cvt_f32_fp8_sdwa v98, v56 src0_sel:BYTE_2
	v_cvt_f32_fp8_sdwa v99, v56 src0_sel:BYTE_3
	v_cvt_f32_fp8_e32 v100, v57
	v_cvt_f32_fp8_sdwa v101, v57 src0_sel:BYTE_1
	v_cvt_f32_fp8_sdwa v102, v57 src0_sel:BYTE_2
	v_cvt_f32_fp8_sdwa v103, v57 src0_sel:BYTE_3
	v_pk_add_f32 v[64:65], v[64:65], v[96:97]
	v_pk_add_f32 v[66:67], v[66:67], v[98:99]
	v_pk_add_f32 v[68:69], v[68:69], v[100:101]
	v_pk_add_f32 v[70:71], v[70:71], v[102:103]
	s_waitcnt vmcnt(14)
; __device__ __forceinline__ void p12_final(const Frame& F, const KArgs& a) {
;     ...
;         for (int j = 0; j < 8; ++j) { const int c = 4 * (lane + 64 * j); { const u32x2 xr = *(const u32x2*)(X2 + (size_t)row * DM + c); v[j] = (f32x4){__builtin_bit_cast(float, xr.x << 16), __builtin_bit_cast(float, xr.x & 0xffff0000u), __builtin_bit_cast(float, xr.y << 16), __builtin_bit_cast(float, xr.y & 0xffff0000u)}; }
; #pragma unroll
;             for (int k = 0; k < 4; ++k) { const int y = *(const int*)(YB + so[k] + c);
;                 v[j][0] += __builtin_amdgcn_cvt_f32_fp8(y, 0); v[j][1] += __builtin_amdgcn_cvt_f32_fp8(y, 1); v[j][2] += __builtin_amdgcn_cvt_f32_fp8(y, 2); v[j][3] += __builtin_amdgcn_cvt_f32_fp8(y, 3); }
;             q += (v[j][0] * v[j][0] + v[j][1] * v[j][1]) + (v[j][2] * v[j][2] + v[j][3] * v[j][3]); }
	v_cvt_f32_fp8_e32 v96, v34
	v_cvt_f32_fp8_sdwa v97, v34 src0_sel:BYTE_1
	v_cvt_f32_fp8_sdwa v98, v34 src0_sel:BYTE_2
	v_cvt_f32_fp8_sdwa v99, v34 src0_sel:BYTE_3
	v_cvt_f32_fp8_e32 v100, v35
	v_cvt_f32_fp8_sdwa v101, v35 src0_sel:BYTE_1
	v_cvt_f32_fp8_sdwa v102, v35 src0_sel:BYTE_2
	v_cvt_f32_fp8_sdwa v103, v35 src0_sel:BYTE_3
	v_pk_add_f32 v[72:73], v[72:73], v[96:97]
	v_pk_add_f32 v[74:75], v[74:75], v[98:99]
	v_pk_add_f32 v[76:77], v[76:77], v[100:101]
	v_pk_add_f32 v[78:79], v[78:79], v[102:103]
	v_cvt_f32_fp8_e32 v96, v42
	v_cvt_f32_fp8_sdwa v97, v42 src0_sel:BYTE_1
	v_cvt_f32_fp8_sdwa v98, v42 src0_sel:BYTE_2
	v_cvt_f32_fp8_sdwa v99, v42 src0_sel:BYTE_3
	v_cvt_f32_fp8_e32 v100, v43
	v_cvt_f32_fp8_sdwa v101, v43 src0_sel:BYTE_1
	v_cvt_f32_fp8_sdwa v102, v43 src0_sel:BYTE_2
	v_cvt_f32_fp8_sdwa v103, v43 src0_sel:BYTE_3
	v_pk_add_f32 v[72:73], v[72:73], v[96:97]
	v_pk_add_f32 v[74:75], v[74:75], v[98:99]
	v_pk_add_f32 v[76:77], v[76:77], v[100:101]
	v_pk_add_f32 v[78:79], v[78:79], v[102:103]
	v_cvt_f32_fp8_e32 v96, v50
	v_cvt_f32_fp8_sdwa v97, v50 src0_sel:BYTE_1
	v_cvt_f32_fp8_sdwa v98, v50 src0_sel:BYTE_2
	v_cvt_f32_fp8_sdwa v99, v50 src0_sel:BYTE_3
	v_cvt_f32_fp8_e32 v100, v51
	v_cvt_f32_fp8_sdwa v101, v51 src0_sel:BYTE_1
	v_cvt_f32_fp8_sdwa v102, v51 src0_sel:BYTE_2
	v_cvt_f32_fp8_sdwa v103, v51 src0_sel:BYTE_3
	v_pk_add_f32 v[72:73], v[72:73], v[96:97]
	v_pk_add_f32 v[74:75], v[74:75], v[98:99]
	v_pk_add_f32 v[76:77], v[76:77], v[100:101]
	v_pk_add_f32 v[78:79], v[78:79], v[102:103]
	v_cvt_f32_fp8_e32 v96, v58
	v_cvt_f32_fp8_sdwa v97, v58 src0_sel:BYTE_1
	v_cvt_f32_fp8_sdwa v98, v58 src0_sel:BYTE_2
	v_cvt_f32_fp8_sdwa v99, v58 src0_sel:BYTE_3
	v_cvt_f32_fp8_e32 v100, v59
	v_cvt_f32_fp8_sdwa v101, v59 src0_sel:BYTE_1
	v_cvt_f32_fp8_sdwa v102, v59 src0_sel:BYTE_2
	v_cvt_f32_fp8_sdwa v103, v59 src0_sel:BYTE_3
	v_pk_add_f32 v[72:73], v[72:73], v[96:97]
	v_pk_add_f32 v[74:75], v[74:75], v[98:99]
	v_pk_add_f32 v[76:77], v[76:77], v[100:101]
	v_pk_add_f32 v[78:79], v[78:79], v[102:103]
	s_waitcnt vmcnt(10)
	v_cvt_f32_fp8_e32 v96, v36
	v_cvt_f32_fp8_sdwa v97, v36 src0_sel:BYTE_1
	v_cvt_f32_fp8_sdwa v98, v36 src0_sel:BYTE_2
	v_cvt_f32_fp8_sdwa v99, v36 src0_sel:BYTE_3
	v_cvt_f32_fp8_e32 v100, v37
	v_cvt_f32_fp8_sdwa v101, v37 src0_sel:BYTE_1
	v_cvt_f32_fp8_sdwa v102, v37 src0_sel:BYTE_2
	v_cvt_f32_fp8_sdwa v103, v37 src0_sel:BYTE_3
	v_pk_add_f32 v[80:81], v[80:81], v[96:97]
	v_pk_add_f32 v[82:83], v[82:83], v[98:99]
	v_pk_add_f32 v[84:85], v[84:85], v[100:101]
	v_pk_add_f32 v[86:87], v[86:87], v[102:103]
	v_cvt_f32_fp8_e32 v96, v44
	v_cvt_f32_fp8_sdwa v97, v44 src0_sel:BYTE_1
	v_cvt_f32_fp8_sdwa v98, v44 src0_sel:BYTE_2
	v_cvt_f32_fp8_sdwa v99, v44 src0_sel:BYTE_3
	v_cvt_f32_fp8_e32 v100, v45
	v_cvt_f32_fp8_sdwa v101, v45 src0_sel:BYTE_1
	v_cvt_f32_fp8_sdwa v102, v45 src0_sel:BYTE_2
	v_cvt_f32_fp8_sdwa v103, v45 src0_sel:BYTE_3
	v_pk_add_f32 v[80:81], v[80:81], v[96:97]
	v_pk_add_f32 v[82:83], v[82:83], v[98:99]
	v_pk_add_f32 v[84:85], v[84:85], v[100:101]
	v_pk_add_f32 v[86:87], v[86:87], v[102:103]
	v_cvt_f32_fp8_e32 v96, v52
	v_cvt_f32_fp8_sdwa v97, v52 src0_sel:BYTE_1
	v_cvt_f32_fp8_sdwa v98, v52 src0_sel:BYTE_2
	v_cvt_f32_fp8_sdwa v99, v52 src0_sel:BYTE_3
	v_cvt_f32_fp8_e32 v100, v53
	v_cvt_f32_fp8_sdwa v101, v53 src0_sel:BYTE_1
	v_cvt_f32_fp8_sdwa v102, v53 src0_sel:BYTE_2
	v_cvt_f32_fp8_sdwa v103, v53 src0_sel:BYTE_3
	v_pk_add_f32 v[80:81], v[80:81], v[96:97]
	v_pk_add_f32 v[82:83], v[82:83], v[98:99]
	v_pk_add_f32 v[84:85], v[84:85], v[100:101]
	v_pk_add_f32 v[86:87], v[86:87], v[102:103]
	v_cvt_f32_fp8_e32 v96, v60
	v_cvt_f32_fp8_sdwa v97, v60 src0_sel:BYTE_1
	v_cvt_f32_fp8_sdwa v98, v60 src0_sel:BYTE_2
	v_cvt_f32_fp8_sdwa v99, v60 src0_sel:BYTE_3
	v_cvt_f32_fp8_e32 v100, v61
	v_cvt_f32_fp8_sdwa v101, v61 src0_sel:BYTE_1
	v_cvt_f32_fp8_sdwa v102, v61 src0_sel:BYTE_2
	v_cvt_f32_fp8_sdwa v103, v61 src0_sel:BYTE_3
	v_pk_add_f32 v[80:81], v[80:81], v[96:97]
	v_pk_add_f32 v[82:83], v[82:83], v[98:99]
	v_pk_add_f32 v[84:85], v[84:85], v[100:101]
	v_pk_add_f32 v[86:87], v[86:87], v[102:103]
	s_waitcnt vmcnt(6)
; __device__ __forceinline__ void p12_final(const Frame& F, const KArgs& a) {
;     ...
;         for (int j = 0; j < 8; ++j) { const int c = 4 * (lane + 64 * j); { const u32x2 xr = *(const u32x2*)(X2 + (size_t)row * DM + c); v[j] = (f32x4){__builtin_bit_cast(float, xr.x << 16), __builtin_bit_cast(float, xr.x & 0xffff0000u), __builtin_bit_cast(float, xr.y << 16), __builtin_bit_cast(float, xr.y & 0xffff0000u)}; }
; #pragma unroll
;             for (int k = 0; k < 4; ++k) { const int y = *(const int*)(YB + so[k] + c);
;                 v[j][0] += __builtin_amdgcn_cvt_f32_fp8(y, 0); v[j][1] += __builtin_amdgcn_cvt_f32_fp8(y, 1); v[j][2] += __builtin_amdgcn_cvt_f32_fp8(y, 2); v[j][3] += __builtin_amdgcn_cvt_f32_fp8(y, 3); }
;             q += (v[j][0] * v[j][0] + v[j][1] * v[j][1]) + (v[j][2] * v[j][2] + v[j][3] * v[j][3]); }
;         const float rs = rsqrtf(wave_sum(q) * (1.f / DM) + RMS_EPS);
; #pragma unroll
;         for (int j = 0; j < 8; ++j) { const int c = 4 * (lane + 64 * j); const f32x4 g = *(const f32x4*)(a.in[24] + c); *(f32x4*)(a.out + (size_t)row * DM + c) = v[j] * rs * g; }
;     }
	v_cvt_f32_fp8_e32 v96, v38
	v_cvt_f32_fp8_sdwa v97, v38 src0_sel:BYTE_1
	v_cvt_f32_fp8_sdwa v98, v38 src0_sel:BYTE_2
	v_cvt_f32_fp8_sdwa v99, v38 src0_sel:BYTE_3
	v_cvt_f32_fp8_e32 v100, v39
	v_cvt_f32_fp8_sdwa v101, v39 src0_sel:BYTE_1
	v_cvt_f32_fp8_sdwa v102, v39 src0_sel:BYTE_2
	v_cvt_f32_fp8_sdwa v103, v39 src0_sel:BYTE_3
	v_pk_add_f32 v[88:89], v[88:89], v[96:97]
	v_pk_add_f32 v[90:91], v[90:91], v[98:99]
	v_pk_add_f32 v[92:93], v[92:93], v[100:101]
	v_pk_add_f32 v[94:95], v[94:95], v[102:103]
	v_cvt_f32_fp8_e32 v96, v46
	v_cvt_f32_fp8_sdwa v97, v46 src0_sel:BYTE_1
	v_cvt_f32_fp8_sdwa v98, v46 src0_sel:BYTE_2
	v_cvt_f32_fp8_sdwa v99, v46 src0_sel:BYTE_3
	v_cvt_f32_fp8_e32 v100, v47
	v_cvt_f32_fp8_sdwa v101, v47 src0_sel:BYTE_1
	v_cvt_f32_fp8_sdwa v102, v47 src0_sel:BYTE_2
	v_cvt_f32_fp8_sdwa v103, v47 src0_sel:BYTE_3
	v_pk_add_f32 v[88:89], v[88:89], v[96:97]
	v_pk_add_f32 v[90:91], v[90:91], v[98:99]
	v_pk_add_f32 v[92:93], v[92:93], v[100:101]
	v_pk_add_f32 v[94:95], v[94:95], v[102:103]
	v_cvt_f32_fp8_e32 v96, v54
	v_cvt_f32_fp8_sdwa v97, v54 src0_sel:BYTE_1
	v_cvt_f32_fp8_sdwa v98, v54 src0_sel:BYTE_2
	v_cvt_f32_fp8_sdwa v99, v54 src0_sel:BYTE_3
	v_cvt_f32_fp8_e32 v100, v55
	v_cvt_f32_fp8_sdwa v101, v55 src0_sel:BYTE_1
	v_cvt_f32_fp8_sdwa v102, v55 src0_sel:BYTE_2
	v_cvt_f32_fp8_sdwa v103, v55 src0_sel:BYTE_3
	v_pk_add_f32 v[88:89], v[88:89], v[96:97]
	v_pk_add_f32 v[90:91], v[90:91], v[98:99]
	v_pk_add_f32 v[92:93], v[92:93], v[100:101]
	v_pk_add_f32 v[94:95], v[94:95], v[102:103]
	v_cvt_f32_fp8_e32 v96, v62
	v_cvt_f32_fp8_sdwa v97, v62 src0_sel:BYTE_1
	v_cvt_f32_fp8_sdwa v98, v62 src0_sel:BYTE_2
	v_cvt_f32_fp8_sdwa v99, v62 src0_sel:BYTE_3
	v_cvt_f32_fp8_e32 v100, v63
	v_cvt_f32_fp8_sdwa v101, v63 src0_sel:BYTE_1
	v_cvt_f32_fp8_sdwa v102, v63 src0_sel:BYTE_2
	v_cvt_f32_fp8_sdwa v103, v63 src0_sel:BYTE_3
	v_pk_add_f32 v[88:89], v[88:89], v[96:97]
	v_pk_add_f32 v[90:91], v[90:91], v[98:99]
	v_pk_add_f32 v[92:93], v[92:93], v[100:101]
	v_pk_add_f32 v[94:95], v[94:95], v[102:103]
	v_pk_mul_f32 v[106:107], v[64:65], v[64:65]
	v_pk_fma_f32 v[106:107], v[66:67], v[66:67], v[106:107]
	v_pk_fma_f32 v[106:107], v[68:69], v[68:69], v[106:107]
	v_pk_fma_f32 v[106:107], v[70:71], v[70:71], v[106:107]
	v_pk_fma_f32 v[106:107], v[72:73], v[72:73], v[106:107]
	v_pk_fma_f32 v[106:107], v[74:75], v[74:75], v[106:107]
	v_pk_fma_f32 v[106:107], v[76:77], v[76:77], v[106:107]
	v_pk_fma_f32 v[106:107], v[78:79], v[78:79], v[106:107]
	v_pk_fma_f32 v[106:107], v[80:81], v[80:81], v[106:107]
	v_pk_fma_f32 v[106:107], v[82:83], v[82:83], v[106:107]
	v_pk_fma_f32 v[106:107], v[84:85], v[84:85], v[106:107]
	v_pk_fma_f32 v[106:107], v[86:87], v[86:87], v[106:107]
	v_pk_fma_f32 v[106:107], v[88:89], v[88:89], v[106:107]
	v_pk_fma_f32 v[106:107], v[90:91], v[90:91], v[106:107]
	v_pk_fma_f32 v[106:107], v[92:93], v[92:93], v[106:107]
	v_pk_fma_f32 v[106:107], v[94:95], v[94:95], v[106:107]
	s_nop 0
	v_add_f32_e32 v105, v106, v107
	s_nop 1
	v_add_f32_dpp v105, v105, v105 quad_perm:[1,0,3,2] row_mask:0xf bank_mask:0xf
	s_nop 1
	v_add_f32_dpp v105, v105, v105 quad_perm:[2,3,0,1] row_mask:0xf bank_mask:0xf
	s_nop 1
	v_add_f32_dpp v105, v105, v105 row_half_mirror row_mask:0xf bank_mask:0xf
	s_nop 1
	v_add_f32_dpp v105, v105, v105 row_mirror row_mask:0xf bank_mask:0xf
	s_nop 1
	v_readlane_b32 s12, v105, 0
	v_readlane_b32 s14, v105, 16
	v_readlane_b32 s15, v105, 32
	v_readlane_b32 s16, v105, 48
	s_nop 1
	v_mov_b32_e32 v105, s12
	v_add_f32_e32 v105, s14, v105
	v_add_f32_e32 v105, s15, v105
	v_add_f32_e32 v105, s16, v105
	v_fmamk_f32 v105, v105, 0x3a000000, v104
	v_rsq_f32_e32 v108, v105
	s_nop 0
	v_pk_mul_f32 v[64:65], v[64:65], v[108:109] op_sel_hi:[1,0]
	v_pk_mul_f32 v[66:67], v[66:67], v[108:109] op_sel_hi:[1,0]
	v_pk_mul_f32 v[68:69], v[68:69], v[108:109] op_sel_hi:[1,0]
	v_pk_mul_f32 v[70:71], v[70:71], v[108:109] op_sel_hi:[1,0]
	v_pk_mul_f32 v[64:65], v[64:65], v[200:201]
	v_pk_mul_f32 v[66:67], v[66:67], v[202:203]
	v_pk_mul_f32 v[68:69], v[68:69], v[204:205]
	v_pk_mul_f32 v[70:71], v[70:71], v[206:207]
	global_store_dwordx4 v4, v[64:67], s[18:19]
	global_store_dwordx4 v4, v[68:71], s[18:19] offset:16
	v_pk_mul_f32 v[72:73], v[72:73], v[108:109] op_sel_hi:[1,0]
	v_pk_mul_f32 v[74:75], v[74:75], v[108:109] op_sel_hi:[1,0]
	v_pk_mul_f32 v[76:77], v[76:77], v[108:109] op_sel_hi:[1,0]
	v_pk_mul_f32 v[78:79], v[78:79], v[108:109] op_sel_hi:[1,0]
	v_pk_mul_f32 v[72:73], v[72:73], v[208:209]
	v_pk_mul_f32 v[74:75], v[74:75], v[210:211]
	v_pk_mul_f32 v[76:77], v[76:77], v[212:213]
	v_pk_mul_f32 v[78:79], v[78:79], v[214:215]
	global_store_dwordx4 v4, v[72:75], s[18:19] offset:2048
	global_store_dwordx4 v4, v[76:79], s[18:19] offset:2064
	v_pk_mul_f32 v[80:81], v[80:81], v[108:109] op_sel_hi:[1,0]
	v_pk_mul_f32 v[82:83], v[82:83], v[108:109] op_sel_hi:[1,0]
	v_pk_mul_f32 v[84:85], v[84:85], v[108:109] op_sel_hi:[1,0]
	v_pk_mul_f32 v[86:87], v[86:87], v[108:109] op_sel_hi:[1,0]
	v_pk_mul_f32 v[80:81], v[80:81], v[216:217]
	v_pk_mul_f32 v[82:83], v[82:83], v[218:219]
	v_pk_mul_f32 v[84:85], v[84:85], v[220:221]
	v_pk_mul_f32 v[86:87], v[86:87], v[222:223]
	global_store_dwordx4 v4, v[80:83], s[24:25]
	global_store_dwordx4 v4, v[84:87], s[24:25] offset:16
	v_pk_mul_f32 v[88:89], v[88:89], v[108:109] op_sel_hi:[1,0]
	v_pk_mul_f32 v[90:91], v[90:91], v[108:109] op_sel_hi:[1,0]
	v_pk_mul_f32 v[92:93], v[92:93], v[108:109] op_sel_hi:[1,0]
	v_pk_mul_f32 v[94:95], v[94:95], v[108:109] op_sel_hi:[1,0]
	v_pk_mul_f32 v[88:89], v[88:89], v[224:225]
	v_pk_mul_f32 v[90:91], v[90:91], v[226:227]
	v_pk_mul_f32 v[92:93], v[92:93], v[228:229]
	v_pk_mul_f32 v[94:95], v[94:95], v[230:231]
	global_store_dwordx4 v4, v[88:91], s[24:25] offset:2048
	global_store_dwordx4 v4, v[92:95], s[24:25] offset:2064
	s_mov_b32 s20, s21
	s_cmpk_lt_i32 s20, 0x4000
	s_cbranch_scc1 .Lp12_row
